# plus index task loads hoisted above the hist-zero barrier and LN0 router-weight staging loads issued together
# baseline (speedup 1.0000x reference)
.LBB0_408:
	s_bitcmp0_b32 s59, 0
	s_cselect_b32 s6, s2, s52
	s_add_i32 s4, s6, s4
	s_cmpk_gt_i32 s4, 0xfff
	s_cbranch_scc1 .LBB0_407
	s_lshl_b32 s9, s4, 2
	s_sub_i32 s4, 0x3ffc, s9
	s_sub_i32 s6, 0x401c, s9
	s_waitcnt vmcnt(3)
	v_or_b32_e32 v18, s4, v133
	v_mov_b64_e32 v[16:17], s[0:1]
	s_movk_i32 s10, 0x2200
	s_lshr_b32 s8, s6, 5
	v_mad_u64_u32 v[0:1], s[6:7], v18, s10, v[16:17]
	v_mov_b32_e32 v127, v137
	v_lshl_add_u64 v[0:1], v[0:1], 0, v[126:127]
	v_lshl_add_u64 v[0:1], v[0:1], 0, v[128:129]
	s_mov_b64 s[12:13], 0x24a01800
	s_lshl_b64 s[6:7], s[4:5], 9
	v_lshl_add_u64 v[2:3], v[0:1], 0, s[12:13]
	v_add_co_u32_e32 v0, vcc, 0x24a01000, v0
	s_add_u32 s6, s0, s6
	s_nop 0
	v_addc_co_u32_e32 v1, vcc, 0, v1, vcc
	s_addc_u32 s7, s1, s7
	global_load_dwordx4 v[34:37], v[2:3], off offset:32
	global_load_dwordx4 v[38:41], v[2:3], off offset:64
	global_load_dwordx4 v[42:45], v[0:1], off offset:2048
	global_load_dwordx4 v[46:49], v[2:3], off offset:96
	v_lshl_add_u64 v[0:1], s[6:7], 0, v[130:131]
	s_sub_i32 s6, 0x3ffd, s9
	s_mov_b32 s7, s5
	s_lshl_b64 s[6:7], s[6:7], 9
	s_mov_b64 s[14:15], 0x31200100
	s_mov_b32 s11, 0x31200000
	s_add_u32 s6, s0, s6
	v_lshl_add_u64 v[4:5], v[0:1], 0, s[14:15]
	v_add_co_u32_e32 v0, vcc, s11, v0
	s_addc_u32 s7, s1, s7
	v_or_b32_e32 v18, 2, v18
	v_addc_co_u32_e32 v1, vcc, 0, v1, vcc
	v_lshl_add_u64 v[8:9], s[6:7], 0, v[130:131]
	v_mad_u64_u32 v[16:17], s[6:7], v18, s10, v[16:17]
	v_lshl_add_u64 v[12:13], v[8:9], 0, s[14:15]
	v_add_co_u32_e32 v8, vcc, s11, v8
	v_lshl_add_u64 v[16:17], v[16:17], 0, v[126:127]
	s_nop 0
	v_addc_co_u32_e32 v9, vcc, 0, v9, vcc
	v_lshl_add_u64 v[16:17], v[16:17], 0, v[128:129]
	s_mov_b32 s6, 0x24a01000
	v_lshl_add_u64 v[18:19], v[16:17], 0, s[12:13]
	v_add_co_u32_e32 v16, vcc, s6, v16
	s_sub_i32 s6, 0x3ffe, s9
	s_mov_b32 s7, s5
	s_lshl_b64 s[6:7], s[6:7], 9
	s_add_u32 s6, s0, s6
	v_addc_co_u32_e32 v17, vcc, 0, v17, vcc
	s_addc_u32 s7, s1, s7
	global_load_dwordx4 v[0:3], v[0:1], off offset:256
	s_nop 0
	global_load_dwordx4 v[4:7], v[4:5], off offset:32
	s_nop 0
	global_load_dwordx4 v[8:11], v[8:9], off offset:256
	s_nop 0
	global_load_dwordx4 v[12:15], v[12:13], off offset:32
	s_nop 0
	global_load_dwordx4 v[50:53], v[18:19], off offset:32
	global_load_dwordx4 v[54:57], v[18:19], off offset:64
	global_load_dwordx4 v[58:61], v[16:17], off offset:2048
	global_load_dwordx4 v[62:65], v[18:19], off offset:96
	v_lshl_add_u64 v[16:17], s[6:7], 0, v[130:131]
	s_sub_i32 s6, 0x3fff, s9
	s_mov_b32 s7, s5
	s_lshl_b64 s[6:7], s[6:7], 9
	s_add_u32 s6, s0, s6
	s_waitcnt vmcnt(14)
	v_lshl_add_u64 v[20:21], v[16:17], 0, s[14:15]
	v_add_co_u32_e32 v16, vcc, s11, v16
	s_addc_u32 s7, s1, s7
	s_nop 0
	v_addc_co_u32_e32 v17, vcc, 0, v17, vcc
	s_waitcnt vmcnt(13)
	v_lshl_add_u64 v[24:25], s[6:7], 0, v[130:131]
	v_lshl_add_u64 v[28:29], v[24:25], 0, s[14:15]
	v_add_co_u32_e32 v24, vcc, 0x31200000, v24
	global_load_dwordx4 v[16:19], v[16:17], off offset:256
	s_nop 0
	global_load_dwordx4 v[20:23], v[20:21], off offset:32
	v_addc_co_u32_e32 v25, vcc, 0, v25, vcc
	global_load_dwordx4 v[24:27], v[24:25], off offset:256
	s_nop 0
	global_load_dwordx4 v[98:101], v[28:29], off offset:32
	s_barrier
	s_and_saveexec_b64 s[42:43], s[36:37]
	s_cbranch_execz .Lzl_done
	s_mov_b64 s[44:45], 0
	v_mov_b32_e32 v204, v152
	v_mov_b32_e32 v205, v151
.Lzl_loop:
	v_add_u32_e32 v205, 0x200, v205
	s_movk_i32 s46, 0xa00
	v_cmp_lt_i32_e32 vcc, s46, v205
	ds_write_b32 v204, v137
	s_or_b64 s[44:45], vcc, s[44:45]
	v_add_u32_e32 v204, 0x800, v204
	s_andn2_b64 exec, exec, s[44:45]
	s_cbranch_execnz .Lzl_loop
.Lzl_done:
	s_or_b64 exec, exec, s[42:43]
	s_cmp_gt_i32 s8, s48
	s_waitcnt lgkmcnt(0)
	s_barrier
	s_cbranch_scc0 .LBB0_434
	s_sub_i32 s6, s8, s48
	s_add_i32 s6, s6, 7
	s_cmp_lt_u32 s6, 8
	s_cbranch_scc1 .LBB0_434
	s_add_i32 s8, s8, -1
	s_min_i32 s7, s58, s8
	s_lshl_b32 s10, s7, 2
	s_or_b32 s12, s10, 3
	s_ashr_i32 s13, s12, 31
	s_lshl_b64 s[12:13], s[12:13], 10
	v_lshl_add_u64 v[28:29], v[116:117], 0, s[12:13]
	s_or_b32 s12, s10, 2
	s_ashr_i32 s13, s12, 31
	s_lshl_b64 s[12:13], s[12:13], 10
	v_lshl_add_u64 v[70:71], v[116:117], 0, s[12:13]
	s_or_b32 s12, s10, 1
	s_ashr_i32 s13, s12, 31
	s_ashr_i32 s11, s10, 31
	s_lshl_b64 s[12:13], s[12:13], 10
	s_lshl_b64 s[10:11], s[10:11], 10
	global_load_dwordx4 v[66:69], v[28:29], off
	s_nop 0
	global_load_dwordx4 v[70:73], v[70:71], off
	v_lshl_add_u64 v[28:29], v[116:117], 0, s[12:13]
	v_lshl_add_u64 v[74:75], v[116:117], 0, s[10:11]
	global_load_dwordx4 v[78:81], v[28:29], off
	global_load_dwordx4 v[90:93], v[74:75], off
	s_nop 0
	global_load_dwordx4 v[74:77], v[118:119], off
	global_load_dwordx4 v[82:85], v[120:121], off
	global_load_dwordx4 v[86:89], v[122:123], off
	global_load_dwordx4 v[94:97], v[124:125], off
	s_waitcnt vmcnt(19)
	v_mul_f32_e32 v127, 0x3c800000, v0
	s_waitcnt vmcnt(18)
	v_mul_f32_e32 v136, 0x3c800000, v4
	v_mul_f32_e32 v155, 0x3c800000, v1
	v_mul_f32_e32 v156, 0x3c800000, v5
	v_mul_f32_e32 v157, 0x3c800000, v2
	v_mul_f32_e32 v158, 0x3c800000, v6
	v_mul_f32_e32 v159, 0x3c800000, v3
	v_mul_f32_e32 v160, 0x3c800000, v7
	s_waitcnt vmcnt(17)
	v_mul_f32_e32 v161, 0x3c800000, v8
	s_waitcnt vmcnt(16)
	v_mul_f32_e32 v162, 0x3c800000, v12
	v_mul_f32_e32 v163, 0x3c800000, v9
	v_mul_f32_e32 v164, 0x3c800000, v13
	v_mul_f32_e32 v165, 0x3c800000, v10
	v_mul_f32_e32 v166, 0x3c800000, v14
	v_mul_f32_e32 v167, 0x3c800000, v11
	v_mul_f32_e32 v168, 0x3c800000, v15
	s_waitcnt vmcnt(11)
	v_mul_f32_e32 v169, 0x3c800000, v16
	s_waitcnt vmcnt(10)
	v_mul_f32_e32 v170, 0x3c800000, v20
	v_mul_f32_e32 v171, 0x3c800000, v17
	v_mul_f32_e32 v172, 0x3c800000, v21
	v_mul_f32_e32 v173, 0x3c800000, v18
	v_mul_f32_e32 v174, 0x3c800000, v22
	v_mul_f32_e32 v175, 0x3c800000, v19
	v_mul_f32_e32 v176, 0x3c800000, v23
	s_waitcnt vmcnt(9)
	v_mul_f32_e32 v177, 0x3c800000, v24
	s_waitcnt vmcnt(8)
	v_mul_f32_e32 v178, 0x3c800000, v98
	v_mul_f32_e32 v179, 0x3c800000, v25
	v_mul_f32_e32 v180, 0x3c800000, v99
	v_mul_f32_e32 v181, 0x3c800000, v26
	v_mul_f32_e32 v182, 0x3c800000, v100
	v_mul_f32_e32 v183, 0x3c800000, v27
	v_mul_f32_e32 v184, 0x3c800000, v101
	s_lshr_b32 s9, s6, 3
	s_min_i32 s6, s57, s8
	v_add_u32_e32 v185, s4, v132
	v_add_u32_e32 v201, s4, v148
	s_mov_b32 s11, 0
	s_mov_b32 s10, s21
	v_mov_b32_e32 v202, v154
	v_mov_b32_e32 v203, v153

.LBB0_1217:
	v_mov_b32_e32 v6, v5
	v_ashrrev_i32_e32 v10, 2, v6
	v_ashrrev_i32_e32 v11, 31, v10
	v_lshlrev_b64 v[8:9], 6, v[10:11]
	v_lshl_add_u64 v[8:9], v[2:3], 0, v[8:9]
	global_load_dwordx4 v[204:207], v[8:9], off
	v_add_u32_e32 v6, 0x200, v5
	v_ashrrev_i32_e32 v10, 2, v6
	v_ashrrev_i32_e32 v11, 31, v10
	v_lshlrev_b64 v[8:9], 6, v[10:11]
	v_lshl_add_u64 v[8:9], v[2:3], 0, v[8:9]
	global_load_dwordx4 v[208:211], v[8:9], off
	v_add_u32_e32 v6, 0x400, v5
	v_ashrrev_i32_e32 v10, 2, v6
	v_ashrrev_i32_e32 v11, 31, v10
	v_lshlrev_b64 v[8:9], 6, v[10:11]
	v_lshl_add_u64 v[8:9], v[2:3], 0, v[8:9]
	global_load_dwordx4 v[212:215], v[8:9], off
	v_add_u32_e32 v6, 0x600, v5
	v_ashrrev_i32_e32 v10, 2, v6
	v_ashrrev_i32_e32 v11, 31, v10
	v_lshlrev_b64 v[8:9], 6, v[10:11]
	v_lshl_add_u64 v[8:9], v[2:3], 0, v[8:9]
	global_load_dwordx4 v[216:219], v[8:9], off
	v_add_u32_e32 v6, 0x800, v5
	v_ashrrev_i32_e32 v10, 2, v6
	v_ashrrev_i32_e32 v11, 31, v10
	v_lshlrev_b64 v[8:9], 6, v[10:11]
	v_lshl_add_u64 v[8:9], v[2:3], 0, v[8:9]
	global_load_dwordx4 v[220:223], v[8:9], off
	v_add_u32_e32 v6, 0xa00, v5
	v_ashrrev_i32_e32 v10, 2, v6
	v_ashrrev_i32_e32 v11, 31, v10
	v_lshlrev_b64 v[8:9], 6, v[10:11]
	v_lshl_add_u64 v[8:9], v[2:3], 0, v[8:9]
	global_load_dwordx4 v[224:227], v[8:9], off
	v_add_u32_e32 v6, 0xc00, v5
	v_ashrrev_i32_e32 v10, 2, v6
	v_ashrrev_i32_e32 v11, 31, v10
	v_lshlrev_b64 v[8:9], 6, v[10:11]
	v_lshl_add_u64 v[8:9], v[2:3], 0, v[8:9]
	global_load_dwordx4 v[228:231], v[8:9], off
	v_add_u32_e32 v6, 0xe00, v5
	v_ashrrev_i32_e32 v10, 2, v6
	v_ashrrev_i32_e32 v11, 31, v10
	v_lshlrev_b64 v[8:9], 6, v[10:11]
	v_lshl_add_u64 v[8:9], v[2:3], 0, v[8:9]
	global_load_dwordx4 v[232:235], v[8:9], off
	v_add_u32_e32 v6, 0x1000, v5
	v_ashrrev_i32_e32 v10, 2, v6
	v_ashrrev_i32_e32 v11, 31, v10
	v_lshlrev_b64 v[8:9], 6, v[10:11]
	v_lshl_add_u64 v[8:9], v[2:3], 0, v[8:9]
	global_load_dwordx4 v[236:239], v[8:9], off
	v_add_u32_e32 v6, 0x1200, v5
	v_ashrrev_i32_e32 v10, 2, v6
	v_ashrrev_i32_e32 v11, 31, v10
	v_lshlrev_b64 v[8:9], 6, v[10:11]
	v_lshl_add_u64 v[8:9], v[2:3], 0, v[8:9]
	global_load_dwordx4 v[160:163], v[8:9], off
	v_add_u32_e32 v6, 0x1400, v5
	v_ashrrev_i32_e32 v10, 2, v6
	v_ashrrev_i32_e32 v11, 31, v10
	v_lshlrev_b64 v[8:9], 6, v[10:11]
	v_lshl_add_u64 v[8:9], v[2:3], 0, v[8:9]
	global_load_dwordx4 v[164:167], v[8:9], off
	v_add_u32_e32 v6, 0x1600, v5
	v_ashrrev_i32_e32 v10, 2, v6
	v_ashrrev_i32_e32 v11, 31, v10
	v_lshlrev_b64 v[8:9], 6, v[10:11]
	v_lshl_add_u64 v[8:9], v[2:3], 0, v[8:9]
	global_load_dwordx4 v[168:171], v[8:9], off
	v_add_u32_e32 v6, 0x1800, v5
	v_ashrrev_i32_e32 v10, 2, v6
	v_ashrrev_i32_e32 v11, 31, v10
	v_lshlrev_b64 v[8:9], 6, v[10:11]
	v_lshl_add_u64 v[8:9], v[2:3], 0, v[8:9]
	global_load_dwordx4 v[176:179], v[8:9], off
	v_add_u32_e32 v6, 0x1a00, v5
	v_ashrrev_i32_e32 v10, 2, v6
	v_ashrrev_i32_e32 v11, 31, v10
	v_lshlrev_b64 v[8:9], 6, v[10:11]
	v_lshl_add_u64 v[8:9], v[2:3], 0, v[8:9]
	global_load_dwordx4 v[180:183], v[8:9], off
	v_add_u32_e32 v6, 0x1c00, v5
	v_ashrrev_i32_e32 v10, 2, v6
	v_ashrrev_i32_e32 v11, 31, v10
	v_lshlrev_b64 v[8:9], 6, v[10:11]
	v_lshl_add_u64 v[8:9], v[2:3], 0, v[8:9]
	global_load_dwordx4 v[244:247], v[8:9], off
	v_add_u32_e32 v6, 0x1e00, v5
	v_ashrrev_i32_e32 v10, 2, v6
	v_ashrrev_i32_e32 v11, 31, v10
	v_lshlrev_b64 v[8:9], 6, v[10:11]
	v_lshl_add_u64 v[8:9], v[2:3], 0, v[8:9]
	global_load_dwordx4 v[248:251], v[8:9], off
	v_mov_b32_e32 v6, v5
	v_ashrrev_i32_e32 v10, 2, v6
	v_and_b32_e32 v11, 0xffff800, v6
	v_lshlrev_b32_e32 v10, 12, v10
	v_lshlrev_b32_e32 v11, 4, v11
	v_and_b32_e32 v10, 0x7000, v10
	v_add3_u32 v10, 0, v11, v10
	v_lshrrev_b32_e32 v11, 1, v6
	v_and_b32_e32 v11, 0x3f0, v11
	v_add3_u32 v10, v10, v1, v11
	s_waitcnt vmcnt(15)
	ds_write_b128 v10, v[204:207]
	v_add_u32_e32 v6, 0x200, v5
	v_ashrrev_i32_e32 v10, 2, v6
	v_and_b32_e32 v11, 0xffff800, v6
	v_lshlrev_b32_e32 v10, 12, v10
	v_lshlrev_b32_e32 v11, 4, v11
	v_and_b32_e32 v10, 0x7000, v10
	v_add3_u32 v10, 0, v11, v10
	v_lshrrev_b32_e32 v11, 1, v6
	v_and_b32_e32 v11, 0x3f0, v11
	v_add3_u32 v10, v10, v1, v11
	s_waitcnt vmcnt(14)
	ds_write_b128 v10, v[208:211]
	v_add_u32_e32 v6, 0x400, v5
	v_ashrrev_i32_e32 v10, 2, v6
	v_and_b32_e32 v11, 0xffff800, v6
	v_lshlrev_b32_e32 v10, 12, v10
	v_lshlrev_b32_e32 v11, 4, v11
	v_and_b32_e32 v10, 0x7000, v10
	v_add3_u32 v10, 0, v11, v10
	v_lshrrev_b32_e32 v11, 1, v6
	v_and_b32_e32 v11, 0x3f0, v11
	v_add3_u32 v10, v10, v1, v11
	s_waitcnt vmcnt(13)
	ds_write_b128 v10, v[212:215]
	v_add_u32_e32 v6, 0x600, v5
	v_ashrrev_i32_e32 v10, 2, v6
	v_and_b32_e32 v11, 0xffff800, v6
	v_lshlrev_b32_e32 v10, 12, v10
	v_lshlrev_b32_e32 v11, 4, v11
	v_and_b32_e32 v10, 0x7000, v10
	v_add3_u32 v10, 0, v11, v10
	v_lshrrev_b32_e32 v11, 1, v6
	v_and_b32_e32 v11, 0x3f0, v11
	v_add3_u32 v10, v10, v1, v11
	s_waitcnt vmcnt(12)
	ds_write_b128 v10, v[216:219]
	v_add_u32_e32 v6, 0x800, v5
	v_ashrrev_i32_e32 v10, 2, v6
	v_and_b32_e32 v11, 0xffff800, v6
	v_lshlrev_b32_e32 v10, 12, v10
	v_lshlrev_b32_e32 v11, 4, v11
	v_and_b32_e32 v10, 0x7000, v10
	v_add3_u32 v10, 0, v11, v10
	v_lshrrev_b32_e32 v11, 1, v6
	v_and_b32_e32 v11, 0x3f0, v11
	v_add3_u32 v10, v10, v1, v11
	s_waitcnt vmcnt(11)
	ds_write_b128 v10, v[220:223]
	v_add_u32_e32 v6, 0xa00, v5
	v_ashrrev_i32_e32 v10, 2, v6
	v_and_b32_e32 v11, 0xffff800, v6
	v_lshlrev_b32_e32 v10, 12, v10
	v_lshlrev_b32_e32 v11, 4, v11
	v_and_b32_e32 v10, 0x7000, v10
	v_add3_u32 v10, 0, v11, v10
	v_lshrrev_b32_e32 v11, 1, v6
	v_and_b32_e32 v11, 0x3f0, v11
	v_add3_u32 v10, v10, v1, v11
	s_waitcnt vmcnt(10)
	ds_write_b128 v10, v[224:227]
	v_add_u32_e32 v6, 0xc00, v5
	v_ashrrev_i32_e32 v10, 2, v6
	v_and_b32_e32 v11, 0xffff800, v6
	v_lshlrev_b32_e32 v10, 12, v10
	v_lshlrev_b32_e32 v11, 4, v11
	v_and_b32_e32 v10, 0x7000, v10
	v_add3_u32 v10, 0, v11, v10
	v_lshrrev_b32_e32 v11, 1, v6
	v_and_b32_e32 v11, 0x3f0, v11
	v_add3_u32 v10, v10, v1, v11
	s_waitcnt vmcnt(9)
	ds_write_b128 v10, v[228:231]
	v_add_u32_e32 v6, 0xe00, v5
	v_ashrrev_i32_e32 v10, 2, v6
	v_and_b32_e32 v11, 0xffff800, v6
	v_lshlrev_b32_e32 v10, 12, v10
	v_lshlrev_b32_e32 v11, 4, v11
	v_and_b32_e32 v10, 0x7000, v10
	v_add3_u32 v10, 0, v11, v10
	v_lshrrev_b32_e32 v11, 1, v6
	v_and_b32_e32 v11, 0x3f0, v11
	v_add3_u32 v10, v10, v1, v11
	s_waitcnt vmcnt(8)
	ds_write_b128 v10, v[232:235]
	v_add_u32_e32 v6, 0x1000, v5
	v_ashrrev_i32_e32 v10, 2, v6
	v_and_b32_e32 v11, 0xffff800, v6
	v_lshlrev_b32_e32 v10, 12, v10
	v_lshlrev_b32_e32 v11, 4, v11
	v_and_b32_e32 v10, 0x7000, v10
	v_add3_u32 v10, 0, v11, v10
	v_lshrrev_b32_e32 v11, 1, v6
	v_and_b32_e32 v11, 0x3f0, v11
	v_add3_u32 v10, v10, v1, v11
	s_waitcnt vmcnt(7)
	ds_write_b128 v10, v[236:239]
	v_add_u32_e32 v6, 0x1200, v5
	v_ashrrev_i32_e32 v10, 2, v6
	v_and_b32_e32 v11, 0xffff800, v6
	v_lshlrev_b32_e32 v10, 12, v10
	v_lshlrev_b32_e32 v11, 4, v11
	v_and_b32_e32 v10, 0x7000, v10
	v_add3_u32 v10, 0, v11, v10
	v_lshrrev_b32_e32 v11, 1, v6
	v_and_b32_e32 v11, 0x3f0, v11
	v_add3_u32 v10, v10, v1, v11
	s_waitcnt vmcnt(6)
	ds_write_b128 v10, v[160:163]
	v_add_u32_e32 v6, 0x1400, v5
	v_ashrrev_i32_e32 v10, 2, v6
	v_and_b32_e32 v11, 0xffff800, v6
	v_lshlrev_b32_e32 v10, 12, v10
	v_lshlrev_b32_e32 v11, 4, v11
	v_and_b32_e32 v10, 0x7000, v10
	v_add3_u32 v10, 0, v11, v10
	v_lshrrev_b32_e32 v11, 1, v6
	v_and_b32_e32 v11, 0x3f0, v11
	v_add3_u32 v10, v10, v1, v11
	s_waitcnt vmcnt(5)
	ds_write_b128 v10, v[164:167]
	v_add_u32_e32 v6, 0x1600, v5
	v_ashrrev_i32_e32 v10, 2, v6
	v_and_b32_e32 v11, 0xffff800, v6
	v_lshlrev_b32_e32 v10, 12, v10
	v_lshlrev_b32_e32 v11, 4, v11
	v_and_b32_e32 v10, 0x7000, v10
	v_add3_u32 v10, 0, v11, v10
	v_lshrrev_b32_e32 v11, 1, v6
	v_and_b32_e32 v11, 0x3f0, v11
	v_add3_u32 v10, v10, v1, v11
	s_waitcnt vmcnt(4)
	ds_write_b128 v10, v[168:171]
	v_add_u32_e32 v6, 0x1800, v5
	v_ashrrev_i32_e32 v10, 2, v6
	v_and_b32_e32 v11, 0xffff800, v6
	v_lshlrev_b32_e32 v10, 12, v10
	v_lshlrev_b32_e32 v11, 4, v11
	v_and_b32_e32 v10, 0x7000, v10
	v_add3_u32 v10, 0, v11, v10
	v_lshrrev_b32_e32 v11, 1, v6
	v_and_b32_e32 v11, 0x3f0, v11
	v_add3_u32 v10, v10, v1, v11
	s_waitcnt vmcnt(3)
	ds_write_b128 v10, v[176:179]
	v_add_u32_e32 v6, 0x1a00, v5
	v_ashrrev_i32_e32 v10, 2, v6
	v_and_b32_e32 v11, 0xffff800, v6
	v_lshlrev_b32_e32 v10, 12, v10
	v_lshlrev_b32_e32 v11, 4, v11
	v_and_b32_e32 v10, 0x7000, v10
	v_add3_u32 v10, 0, v11, v10
	v_lshrrev_b32_e32 v11, 1, v6
	v_and_b32_e32 v11, 0x3f0, v11
	v_add3_u32 v10, v10, v1, v11
	s_waitcnt vmcnt(2)
	ds_write_b128 v10, v[180:183]
	v_add_u32_e32 v6, 0x1c00, v5
	v_ashrrev_i32_e32 v10, 2, v6
	v_and_b32_e32 v11, 0xffff800, v6
	v_lshlrev_b32_e32 v10, 12, v10
	v_lshlrev_b32_e32 v11, 4, v11
	v_and_b32_e32 v10, 0x7000, v10
	v_add3_u32 v10, 0, v11, v10
	v_lshrrev_b32_e32 v11, 1, v6
	v_and_b32_e32 v11, 0x3f0, v11
	v_add3_u32 v10, v10, v1, v11
	s_waitcnt vmcnt(1)
	ds_write_b128 v10, v[244:247]
	v_add_u32_e32 v6, 0x1e00, v5
	v_ashrrev_i32_e32 v10, 2, v6
	v_and_b32_e32 v11, 0xffff800, v6
	v_lshlrev_b32_e32 v10, 12, v10
	v_lshlrev_b32_e32 v11, 4, v11
	v_and_b32_e32 v10, 0x7000, v10
	v_add3_u32 v10, 0, v11, v10
	v_lshrrev_b32_e32 v11, 1, v6
	v_and_b32_e32 v11, 0x3f0, v11
	v_add3_u32 v10, v10, v1, v11
	s_waitcnt vmcnt(0)
	ds_write_b128 v10, v[248:251]
